# P0 expert-weight fp8 stores marked nt (non-temporal)
# speedup vs baseline: 1.0384x; 1.0384x over previous
; #define MOE_LOAD(v, it) do { _Pragma("unroll") for (int i_ = 0; i_ < 64; ++i_) v[i_] = __builtin_nontemporal_load((it).src + (size_t)(2 * i_) * (it).stride); } while (0)
;     ...
;             ia = moe_item(wg, wu, wd, win, wout, wpn, wpd, F.ws, it2 <= last ? it2 : last, F.lane); MOE_LOAD(va, ia);
;             MOE_PROC(vb, ib);
.LBB0_80:
	s_lshl_b64 s[68:69], s[68:69], 3
	v_lshl_add_u64 v[14:15], v[16:17], 0, s[68:69]
	global_load_dword v87, v[16:17], off nt
	v_lshl_add_u64 v[16:17], v[14:15], 0, s[68:69]
	v_lshl_add_u64 v[30:31], v[16:17], 0, s[68:69]
	v_lshl_add_u64 v[32:33], v[30:31], 0, s[68:69]
	v_lshl_add_u64 v[34:35], v[32:33], 0, s[68:69]
	v_lshl_add_u64 v[36:37], v[34:35], 0, s[68:69]
	v_lshl_add_u64 v[38:39], v[36:37], 0, s[68:69]
	v_lshl_add_u64 v[40:41], v[38:39], 0, s[68:69]
	global_load_dword v92, v[14:15], off nt
	global_load_dword v91, v[16:17], off nt
	global_load_dword v90, v[30:31], off nt
	global_load_dword v89, v[32:33], off nt
	global_load_dword v88, v[34:35], off nt
	global_load_dword v86, v[36:37], off nt
	global_load_dword v85, v[38:39], off nt
	global_load_dword v83, v[40:41], off nt
	v_lshl_add_u64 v[14:15], v[40:41], 0, s[68:69]
	v_lshl_add_u64 v[16:17], v[14:15], 0, s[68:69]
	global_load_dword v84, v[14:15], off nt
	global_load_dword v79, v[16:17], off nt
	v_lshl_add_u64 v[14:15], v[16:17], 0, s[68:69]
	global_load_dword v80, v[14:15], off nt
	v_lshl_add_u64 v[14:15], v[14:15], 0, s[68:69]
	global_load_dword v75, v[14:15], off nt
	v_lshl_add_u64 v[14:15], v[14:15], 0, s[68:69]
	global_load_dword v76, v[14:15], off nt
	v_lshl_add_u64 v[14:15], v[14:15], 0, s[68:69]
	global_load_dword v71, v[14:15], off nt
	v_lshl_add_u64 v[14:15], v[14:15], 0, s[68:69]
	global_load_dword v72, v[14:15], off nt
	v_lshl_add_u64 v[14:15], v[14:15], 0, s[68:69]
	global_load_dword v65, v[14:15], off nt
	v_lshl_add_u64 v[14:15], v[14:15], 0, s[68:69]
	global_load_dword v66, v[14:15], off nt
	v_lshl_add_u64 v[14:15], v[14:15], 0, s[68:69]
	global_load_dword v61, v[14:15], off nt
	v_lshl_add_u64 v[14:15], v[14:15], 0, s[68:69]
	global_load_dword v62, v[14:15], off nt
	v_lshl_add_u64 v[14:15], v[14:15], 0, s[68:69]
	global_load_dword v57, v[14:15], off nt
	v_lshl_add_u64 v[14:15], v[14:15], 0, s[68:69]
	global_load_dword v58, v[14:15], off nt
	v_lshl_add_u64 v[14:15], v[14:15], 0, s[68:69]
	global_load_dword v53, v[14:15], off nt
	v_lshl_add_u64 v[14:15], v[14:15], 0, s[68:69]
	global_load_dword v54, v[14:15], off nt
	v_lshl_add_u64 v[14:15], v[14:15], 0, s[68:69]
	global_load_dword v45, v[14:15], off nt
	v_lshl_add_u64 v[14:15], v[14:15], 0, s[68:69]
	global_load_dword v46, v[14:15], off nt
	v_lshl_add_u64 v[14:15], v[14:15], 0, s[68:69]
	global_load_dword v35, v[14:15], off nt
	v_lshl_add_u64 v[14:15], v[14:15], 0, s[68:69]
	global_load_dword v36, v[14:15], off nt
	v_lshl_add_u64 v[14:15], v[14:15], 0, s[68:69]
	global_load_dword v33, v[14:15], off nt
	v_lshl_add_u64 v[14:15], v[14:15], 0, s[68:69]
	global_load_dword v34, v[14:15], off nt
	v_lshl_add_u64 v[14:15], v[14:15], 0, s[68:69]
	global_load_dword v31, v[14:15], off nt
	v_lshl_add_u64 v[14:15], v[14:15], 0, s[68:69]
	global_load_dword v32, v[14:15], off nt
	v_lshl_add_u64 v[14:15], v[14:15], 0, s[68:69]
	global_load_dword v29, v[14:15], off nt
	v_lshl_add_u64 v[14:15], v[14:15], 0, s[68:69]
	global_load_dword v30, v[14:15], off nt
	v_lshl_add_u64 v[14:15], v[14:15], 0, s[68:69]
	global_load_dword v81, v[14:15], off nt
	v_lshl_add_u64 v[14:15], v[14:15], 0, s[68:69]
	global_load_dword v82, v[14:15], off nt
	v_lshl_add_u64 v[14:15], v[14:15], 0, s[68:69]
	global_load_dword v77, v[14:15], off nt
	v_lshl_add_u64 v[14:15], v[14:15], 0, s[68:69]
	global_load_dword v78, v[14:15], off nt
	v_lshl_add_u64 v[14:15], v[14:15], 0, s[68:69]
	global_load_dword v73, v[14:15], off nt
	v_lshl_add_u64 v[14:15], v[14:15], 0, s[68:69]
	global_load_dword v74, v[14:15], off nt
	v_lshl_add_u64 v[14:15], v[14:15], 0, s[68:69]
	global_load_dword v69, v[14:15], off nt
	v_lshl_add_u64 v[14:15], v[14:15], 0, s[68:69]
	global_load_dword v70, v[14:15], off nt
	v_lshl_add_u64 v[14:15], v[14:15], 0, s[68:69]
	global_load_dword v67, v[14:15], off nt
	v_lshl_add_u64 v[14:15], v[14:15], 0, s[68:69]
	global_load_dword v68, v[14:15], off nt
	v_lshl_add_u64 v[14:15], v[14:15], 0, s[68:69]
	global_load_dword v63, v[14:15], off nt
	v_lshl_add_u64 v[14:15], v[14:15], 0, s[68:69]
	global_load_dword v64, v[14:15], off nt
	v_lshl_add_u64 v[14:15], v[14:15], 0, s[68:69]
	global_load_dword v59, v[14:15], off nt
	v_lshl_add_u64 v[14:15], v[14:15], 0, s[68:69]
	global_load_dword v60, v[14:15], off nt
	v_lshl_add_u64 v[14:15], v[14:15], 0, s[68:69]
	global_load_dword v55, v[14:15], off nt
	v_lshl_add_u64 v[14:15], v[14:15], 0, s[68:69]
	global_load_dword v56, v[14:15], off nt
	v_lshl_add_u64 v[14:15], v[14:15], 0, s[68:69]
	global_load_dword v51, v[14:15], off nt
	v_lshl_add_u64 v[14:15], v[14:15], 0, s[68:69]
	global_load_dword v52, v[14:15], off nt
	v_lshl_add_u64 v[14:15], v[14:15], 0, s[68:69]
	global_load_dword v38, v[14:15], off nt
	v_lshl_add_u64 v[14:15], v[14:15], 0, s[68:69]
	global_load_dword v39, v[14:15], off nt
	v_lshl_add_u64 v[14:15], v[14:15], 0, s[68:69]
	global_load_dword v40, v[14:15], off nt
	v_lshl_add_u64 v[14:15], v[14:15], 0, s[68:69]
	global_load_dword v42, v[14:15], off nt
	v_lshl_add_u64 v[14:15], v[14:15], 0, s[68:69]
	global_load_dword v37, v[14:15], off nt
	v_lshl_add_u64 v[14:15], v[14:15], 0, s[68:69]
	global_load_dword v41, v[14:15], off nt
	v_lshl_add_u64 v[14:15], v[14:15], 0, s[68:69]
	global_load_dword v43, v[14:15], off nt
	v_lshl_add_u64 v[14:15], v[14:15], 0, s[68:69]
	global_load_dword v44, v[14:15], off nt
	v_lshl_add_u64 v[14:15], v[14:15], 0, s[68:69]
	global_load_dword v47, v[14:15], off nt
	v_lshl_add_u64 v[14:15], v[14:15], 0, s[68:69]
	global_load_dword v48, v[14:15], off nt
	v_lshl_add_u64 v[14:15], v[14:15], 0, s[68:69]
	global_load_dword v49, v[14:15], off nt
	v_lshl_add_u64 v[14:15], v[14:15], 0, s[68:69]
	s_waitcnt vmcnt(62)
	ds_write2st64_b32 v28, v93, v101 offset1:1
	ds_write2st64_b32 v28, v99, v100 offset0:2 offset1:3
	ds_write2st64_b32 v28, v97, v98 offset0:4 offset1:5
	ds_write2st64_b32 v28, v95, v96 offset0:6 offset1:7
	ds_write2st64_b32 v21, v94, v124 offset0:8 offset1:9
	ds_write2st64_b32 v21, v104, v114 offset0:10 offset1:11
	ds_write2st64_b32 v21, v105, v115 offset0:12 offset1:13
	ds_write2st64_b32 v21, v106, v116 offset0:14 offset1:15
	ds_write2st64_b32 v22, v107, v117 offset0:16 offset1:17
	ds_write2st64_b32 v22, v108, v118 offset0:18 offset1:19
	ds_write2st64_b32 v22, v109, v119 offset0:20 offset1:21
	ds_write2st64_b32 v22, v110, v120 offset0:22 offset1:23
	ds_write2st64_b32 v23, v111, v121 offset0:24 offset1:25
	ds_write2st64_b32 v23, v112, v122 offset0:26 offset1:27
	global_load_dword v50, v[14:15], off nt
	ds_write2st64_b32 v23, v102, v103 offset0:28 offset1:29
	ds_write2st64_b32 v23, v113, v123 offset0:30 offset1:31
	ds_write2st64_b32 v24, v125, v126 offset0:32 offset1:33
	ds_write2st64_b32 v24, v127, v128 offset0:34 offset1:35
	ds_write2st64_b32 v24, v129, v130 offset0:36 offset1:37
	ds_write2st64_b32 v24, v131, v132 offset0:38 offset1:39
	ds_write2st64_b32 v25, v133, v134 offset0:40 offset1:41
	ds_write2st64_b32 v25, v135, v136 offset0:42 offset1:43
	ds_write2st64_b32 v25, v137, v138 offset0:44 offset1:45
	ds_write2st64_b32 v25, v139, v140 offset0:46 offset1:47
	ds_write2st64_b32 v26, v141, v142 offset0:48 offset1:49
	ds_write2st64_b32 v26, v143, v144 offset0:50 offset1:51
	ds_write2st64_b32 v26, v146, v147 offset0:52 offset1:53
	ds_write2st64_b32 v26, v148, v149 offset0:54 offset1:55
	ds_write2st64_b32 v27, v151, v152 offset0:56 offset1:57
	ds_write2st64_b32 v27, v153, v154 offset0:58 offset1:59
	ds_write2st64_b32 v27, v155, v157 offset0:60 offset1:61
	ds_write2st64_b32 v27, v158, v159 offset0:62 offset1:63
	s_waitcnt lgkmcnt(0)
	ds_read2_b32 v[16:17], v1 offset1:32
	v_lshlrev_b64 v[14:15], s44, v[2:3]
	v_lshl_add_u64 v[12:13], v[12:13], 0, v[14:15]
	v_lshl_add_u64 v[98:99], v[12:13], 0, v[6:7]
	v_mov_b32_e32 v12, 0
	s_waitcnt lgkmcnt(0)
	v_mul_f32_e32 v4, 0x42800000, v16
	v_mul_f32_e32 v13, 0x42800000, v17
	ds_read2_b32 v[16:17], v1 offset0:64 offset1:96
	ds_read2_b32 v[94:95], v1 offset0:128 offset1:160
	v_cvt_pk_fp8_f32 v12, v4, v13
	v_lshlrev_b64 v[14:15], s46, v[2:3]
	v_lshl_add_u64 v[10:11], v[10:11], 0, v[14:15]
	s_waitcnt lgkmcnt(1)
	v_mul_f32_e32 v4, 0x42800000, v16
	v_mul_f32_e32 v13, 0x42800000, v17
	v_cvt_pk_fp8_f32 v12, v4, v13 op_sel:[0,0,1]
	s_waitcnt lgkmcnt(0)
	v_mul_f32_e32 v4, 0x42800000, v94
	ds_read2_b32 v[14:15], v1 offset0:192 offset1:224
	v_mul_f32_e32 v16, 0x42800000, v95
	v_mov_b32_e32 v13, 0
	v_cvt_pk_fp8_f32 v13, v4, v16
	ds_read2_b32 v[16:17], v145 offset1:32
	s_waitcnt lgkmcnt(1)
	v_mul_f32_e32 v4, 0x42800000, v14
	v_mul_f32_e32 v93, 0x42800000, v15
	ds_read2_b32 v[14:15], v145 offset0:64 offset1:96
	v_cvt_pk_fp8_f32 v13, v4, v93 op_sel:[0,0,1]
	s_waitcnt lgkmcnt(1)
	v_mul_f32_e32 v4, 0x42800000, v16
	v_mul_f32_e32 v93, 0x42800000, v17
	ds_read2_b32 v[16:17], v145 offset0:128 offset1:160
	s_waitcnt lgkmcnt(1)
	v_mul_f32_e32 v96, 0x42800000, v14
	v_mov_b32_e32 v14, 0
	v_cvt_pk_fp8_f32 v14, v4, v93
	v_mul_f32_e32 v97, 0x42800000, v15
	s_waitcnt lgkmcnt(0)
	v_mul_f32_e32 v4, 0x42800000, v16
	v_mul_f32_e32 v93, 0x42800000, v17
	ds_read2_b32 v[16:17], v145 offset0:192 offset1:224
	v_mov_b32_e32 v15, 0
	v_cvt_pk_fp8_f32 v15, v4, v93
	ds_read2_b32 v[94:95], v9 offset1:32
	v_cvt_pk_fp8_f32 v14, v96, v97 op_sel:[0,0,1]
	s_waitcnt lgkmcnt(1)
	v_mul_f32_e32 v4, 0x42800000, v16
	v_mul_f32_e32 v16, 0x42800000, v17
	v_cvt_pk_fp8_f32 v15, v4, v16 op_sel:[0,0,1]
	ds_read2_b32 v[16:17], v9 offset0:64 offset1:96
	s_waitcnt lgkmcnt(1)
	v_mul_f32_e32 v4, 0x42800000, v94
	v_mul_f32_e32 v93, 0x42800000, v95
	v_mov_b32_e32 v94, 0
	ds_read2_b32 v[96:97], v9 offset0:128 offset1:160
	v_cvt_pk_fp8_f32 v94, v4, v93
	global_store_dwordx4 v[98:99], v[12:15], off nt
	s_waitcnt lgkmcnt(1)
	v_mul_f32_e32 v4, 0x42800000, v16
	v_mov_b32_e32 v95, 0
	v_mul_f32_e32 v12, 0x42800000, v17
	v_cvt_pk_fp8_f32 v94, v4, v12 op_sel:[0,0,1]
	s_waitcnt lgkmcnt(0)
	v_mul_f32_e32 v4, 0x42800000, v96
	ds_read2_b32 v[12:13], v9 offset0:192 offset1:224
	v_mul_f32_e32 v14, 0x42800000, v97
	v_cvt_pk_fp8_f32 v95, v4, v14
	ds_read2_b32 v[14:15], v150 offset1:32
	v_mov_b32_e32 v96, 0
	s_waitcnt lgkmcnt(1)
;     ...
;         for (int j = 0; j < nmine; j += 2) {
	v_mul_f32_e32 v4, 0x42800000, v12
	v_mul_f32_e32 v16, 0x42800000, v13
	ds_read2_b32 v[12:13], v150 offset0:64 offset1:96
	v_cvt_pk_fp8_f32 v95, v4, v16 op_sel:[0,0,1]
	s_waitcnt lgkmcnt(1)
	v_mul_f32_e32 v4, 0x42800000, v14
	v_mul_f32_e32 v16, 0x42800000, v15
	ds_read2_b32 v[14:15], v150 offset0:128 offset1:160
	s_waitcnt lgkmcnt(1)
	v_mul_f32_e32 v17, 0x42800000, v12
	v_mul_f32_e32 v93, 0x42800000, v13
	ds_read2_b32 v[12:13], v150 offset0:192 offset1:224
	v_cvt_pk_fp8_f32 v96, v4, v16
	s_waitcnt lgkmcnt(1)
	v_mul_f32_e32 v4, 0x42800000, v14
	v_mul_f32_e32 v14, 0x42800000, v15
	v_mov_b32_e32 v97, 0
	v_cvt_pk_fp8_f32 v97, v4, v14
	s_waitcnt lgkmcnt(0)
	v_mul_f32_e32 v4, 0x42800000, v12
	v_mul_f32_e32 v12, 0x42800000, v13
	v_cvt_pk_fp8_f32 v96, v17, v93 op_sel:[0,0,1]
	v_cvt_pk_fp8_f32 v97, v4, v12 op_sel:[0,0,1]
	s_lshl_b32 s4, s42, 3
	ds_read2_b32 v[12:13], v18 offset1:32
	v_lshl_add_u64 v[16:17], v[98:99], 0, s[4:5]
	ds_read2_b32 v[14:15], v18 offset0:64 offset1:96
	global_store_dwordx4 v[16:17], v[94:97], off nt
	ds_read2_b32 v[94:95], v18 offset0:128 offset1:160
	s_waitcnt lgkmcnt(2)
	v_mul_f32_e32 v4, 0x42800000, v12
	v_mul_f32_e32 v13, 0x42800000, v13
	v_mov_b32_e32 v12, 0
	s_waitcnt lgkmcnt(1)
	v_mul_f32_e32 v93, 0x42800000, v14
	v_mul_f32_e32 v96, 0x42800000, v15
	v_cvt_pk_fp8_f32 v12, v4, v13
	s_waitcnt lgkmcnt(0)
	v_mul_f32_e32 v4, 0x42800000, v94
	v_mul_f32_e32 v94, 0x42800000, v95
	ds_read2_b32 v[14:15], v18 offset0:192 offset1:224
	v_mov_b32_e32 v13, 0
	v_cvt_pk_fp8_f32 v13, v4, v94
	ds_read2_b32 v[94:95], v156 offset1:32
	v_cvt_pk_fp8_f32 v12, v93, v96 op_sel:[0,0,1]
	s_waitcnt lgkmcnt(1)
	v_mul_f32_e32 v4, 0x42800000, v14
	v_mul_f32_e32 v14, 0x42800000, v15
	ds_read2_b32 v[96:97], v156 offset0:64 offset1:96
	v_cvt_pk_fp8_f32 v13, v4, v14 op_sel:[0,0,1]
	s_waitcnt lgkmcnt(1)
	v_mul_f32_e32 v4, 0x42800000, v94
	v_mul_f32_e32 v15, 0x42800000, v95
	v_mov_b32_e32 v14, 0
	ds_read2_b32 v[94:95], v156 offset0:128 offset1:160
	v_cvt_pk_fp8_f32 v14, v4, v15
	s_waitcnt lgkmcnt(1)
	v_mul_f32_e32 v4, 0x42800000, v96
	v_mul_f32_e32 v15, 0x42800000, v97
	ds_read2_b32 v[96:97], v156 offset0:192 offset1:224
	v_cvt_pk_fp8_f32 v14, v4, v15 op_sel:[0,0,1]
	s_waitcnt lgkmcnt(1)
	v_mul_f32_e32 v4, 0x42800000, v94
	v_mul_f32_e32 v93, 0x42800000, v95
	ds_read2_b32 v[94:95], v19 offset1:32
	s_waitcnt lgkmcnt(1)
	v_mul_f32_e32 v100, 0x42800000, v96
	v_mul_f32_e32 v101, 0x42800000, v97
	v_mov_b32_e32 v15, 0
	ds_read2_b32 v[96:97], v19 offset0:64 offset1:96
	v_cvt_pk_fp8_f32 v15, v4, v93
	s_waitcnt lgkmcnt(1)
	v_mul_f32_e32 v4, 0x42800000, v94
	v_mul_f32_e32 v93, 0x42800000, v95
	v_mov_b32_e32 v94, 0
	ds_read2_b32 v[98:99], v19 offset0:128 offset1:160
	v_cvt_pk_fp8_f32 v94, v4, v93
	s_waitcnt lgkmcnt(1)
	v_mul_f32_e32 v4, 0x42800000, v96
	v_mul_f32_e32 v93, 0x42800000, v97
	ds_read2_b32 v[96:97], v19 offset0:192 offset1:224
	v_cvt_pk_fp8_f32 v94, v4, v93 op_sel:[0,0,1]
	s_waitcnt lgkmcnt(1)
	v_mul_f32_e32 v4, 0x42800000, v98
	v_mul_f32_e32 v93, 0x42800000, v99
	v_mov_b32_e32 v95, 0
	ds_read2_b32 v[98:99], v160 offset1:32
	v_cvt_pk_fp8_f32 v95, v4, v93
	s_waitcnt lgkmcnt(1)
	v_mul_f32_e32 v4, 0x42800000, v96
	v_mul_f32_e32 v93, 0x42800000, v97
	ds_read2_b32 v[96:97], v160 offset0:64 offset1:96
	v_cvt_pk_fp8_f32 v95, v4, v93 op_sel:[0,0,1]
	s_waitcnt lgkmcnt(1)
	v_mul_f32_e32 v4, 0x42800000, v98
	v_mul_f32_e32 v93, 0x42800000, v99
	ds_read2_b32 v[98:99], v160 offset0:128 offset1:160
	v_cvt_pk_fp8_f32 v15, v100, v101 op_sel:[0,0,1]
	s_waitcnt lgkmcnt(1)
	v_mul_f32_e32 v102, 0x42800000, v96
	v_mov_b32_e32 v96, 0
	ds_read2_b32 v[100:101], v160 offset0:192 offset1:224
	v_mul_f32_e32 v103, 0x42800000, v97
	v_cvt_pk_fp8_f32 v96, v4, v93
	s_waitcnt lgkmcnt(1)
	v_mul_f32_e32 v4, 0x42800000, v98
	v_mul_f32_e32 v93, 0x42800000, v99
	v_mov_b32_e32 v97, 0
	v_cvt_pk_fp8_f32 v97, v4, v93
	s_waitcnt lgkmcnt(0)
	v_mul_f32_e32 v4, 0x42800000, v100
	v_mul_f32_e32 v93, 0x42800000, v101
	v_cvt_pk_fp8_f32 v96, v102, v103 op_sel:[0,0,1]
	v_cvt_pk_fp8_f32 v97, v4, v93 op_sel:[0,0,1]
	v_lshl_add_u64 v[16:17], v[16:17], 0, s[4:5]
	global_store_dwordx4 v[16:17], v[12:15], off nt
	s_add_i32 s91, s91, 2
	s_cmp_ge_i32 s91, s6
	v_lshl_add_u64 v[12:13], v[16:17], 0, s[4:5]
	global_store_dwordx4 v[12:13], v[94:97], off nt
	s_waitcnt lgkmcnt(0)
	s_cbranch_scc1 .LBB0_130

; #define MOE_LOAD(v, it) do { _Pragma("unroll") for (int i_ = 0; i_ < 64; ++i_) v[i_] = __builtin_nontemporal_load((it).src + (size_t)(2 * i_) * (it).stride); } while (0)
;     ...
;             ib = moe_item(wg, wu, wd, win, wout, wpn, wpd, F.ws, it1 <= last ? it1 : last, F.lane); MOE_LOAD(vb, ib);
;             MOE_PROC(va, ia);
.LBB0_105:
	s_lshl_b64 s[46:47], s[46:47], 3
	global_load_dword v93, v[16:17], off nt
	v_lshl_add_u64 v[16:17], v[16:17], 0, s[46:47]
	v_lshl_add_u64 v[94:95], v[16:17], 0, s[46:47]
	v_lshl_add_u64 v[96:97], v[94:95], 0, s[46:47]
	v_lshl_add_u64 v[102:103], v[96:97], 0, s[46:47]
	v_lshl_add_u64 v[104:105], v[102:103], 0, s[46:47]
	v_lshl_add_u64 v[106:107], v[104:105], 0, s[46:47]
	v_lshl_add_u64 v[108:109], v[106:107], 0, s[46:47]
	v_lshl_add_u64 v[110:111], v[108:109], 0, s[46:47]
	global_load_dword v101, v[16:17], off nt
	global_load_dword v99, v[94:95], off nt
	global_load_dword v100, v[96:97], off nt
	s_nop 0
	global_load_dword v97, v[102:103], off nt
	global_load_dword v98, v[104:105], off nt
	global_load_dword v95, v[106:107], off nt
	global_load_dword v96, v[108:109], off nt
	global_load_dword v94, v[110:111], off nt
	v_lshl_add_u64 v[16:17], v[110:111], 0, s[46:47]
	s_waitcnt vmcnt(9)
	ds_write2st64_b32 v28, v87, v92 offset1:1
	v_lshl_add_u64 v[102:103], v[16:17], 0, s[46:47]
	global_load_dword v124, v[16:17], off nt
	global_load_dword v104, v[102:103], off nt
	v_lshl_add_u64 v[16:17], v[102:103], 0, s[46:47]
	global_load_dword v114, v[16:17], off nt
	v_lshl_add_u64 v[16:17], v[16:17], 0, s[46:47]
	global_load_dword v105, v[16:17], off nt
	v_lshl_add_u64 v[16:17], v[16:17], 0, s[46:47]
	global_load_dword v115, v[16:17], off nt
	v_lshl_add_u64 v[16:17], v[16:17], 0, s[46:47]
	global_load_dword v106, v[16:17], off nt
	v_lshl_add_u64 v[16:17], v[16:17], 0, s[46:47]
	global_load_dword v116, v[16:17], off nt
	v_lshl_add_u64 v[16:17], v[16:17], 0, s[46:47]
	global_load_dword v107, v[16:17], off nt
	v_lshl_add_u64 v[16:17], v[16:17], 0, s[46:47]
	global_load_dword v117, v[16:17], off nt
	v_lshl_add_u64 v[16:17], v[16:17], 0, s[46:47]
	global_load_dword v108, v[16:17], off nt
	v_lshl_add_u64 v[16:17], v[16:17], 0, s[46:47]
	global_load_dword v118, v[16:17], off nt
	v_lshl_add_u64 v[16:17], v[16:17], 0, s[46:47]
	global_load_dword v109, v[16:17], off nt
	v_lshl_add_u64 v[16:17], v[16:17], 0, s[46:47]
	global_load_dword v119, v[16:17], off nt
	v_lshl_add_u64 v[16:17], v[16:17], 0, s[46:47]
	global_load_dword v110, v[16:17], off nt
	v_lshl_add_u64 v[16:17], v[16:17], 0, s[46:47]
	global_load_dword v120, v[16:17], off nt
	v_lshl_add_u64 v[16:17], v[16:17], 0, s[46:47]
	global_load_dword v111, v[16:17], off nt
	v_lshl_add_u64 v[16:17], v[16:17], 0, s[46:47]
	global_load_dword v121, v[16:17], off nt
	v_lshl_add_u64 v[16:17], v[16:17], 0, s[46:47]
	global_load_dword v112, v[16:17], off nt
	v_lshl_add_u64 v[16:17], v[16:17], 0, s[46:47]
	global_load_dword v122, v[16:17], off nt
	v_lshl_add_u64 v[16:17], v[16:17], 0, s[46:47]
	global_load_dword v102, v[16:17], off nt
	v_lshl_add_u64 v[16:17], v[16:17], 0, s[46:47]
	global_load_dword v103, v[16:17], off nt
	v_lshl_add_u64 v[16:17], v[16:17], 0, s[46:47]
	global_load_dword v113, v[16:17], off nt
	v_lshl_add_u64 v[16:17], v[16:17], 0, s[46:47]
	global_load_dword v123, v[16:17], off nt
	v_lshl_add_u64 v[16:17], v[16:17], 0, s[46:47]
	global_load_dword v125, v[16:17], off nt
	v_lshl_add_u64 v[16:17], v[16:17], 0, s[46:47]
	global_load_dword v126, v[16:17], off nt
	v_lshl_add_u64 v[16:17], v[16:17], 0, s[46:47]
	global_load_dword v127, v[16:17], off nt
	v_lshl_add_u64 v[16:17], v[16:17], 0, s[46:47]
	global_load_dword v128, v[16:17], off nt
	v_lshl_add_u64 v[16:17], v[16:17], 0, s[46:47]
	global_load_dword v129, v[16:17], off nt
	v_lshl_add_u64 v[16:17], v[16:17], 0, s[46:47]
	global_load_dword v130, v[16:17], off nt
	v_lshl_add_u64 v[16:17], v[16:17], 0, s[46:47]
	global_load_dword v131, v[16:17], off nt
	v_lshl_add_u64 v[16:17], v[16:17], 0, s[46:47]
	global_load_dword v132, v[16:17], off nt
	v_lshl_add_u64 v[16:17], v[16:17], 0, s[46:47]
	global_load_dword v133, v[16:17], off nt
	v_lshl_add_u64 v[16:17], v[16:17], 0, s[46:47]
	global_load_dword v134, v[16:17], off nt
	v_lshl_add_u64 v[16:17], v[16:17], 0, s[46:47]
	global_load_dword v135, v[16:17], off nt
	v_lshl_add_u64 v[16:17], v[16:17], 0, s[46:47]
	global_load_dword v136, v[16:17], off nt
	v_lshl_add_u64 v[16:17], v[16:17], 0, s[46:47]
	global_load_dword v137, v[16:17], off nt
	v_lshl_add_u64 v[16:17], v[16:17], 0, s[46:47]
	global_load_dword v138, v[16:17], off nt
	v_lshl_add_u64 v[16:17], v[16:17], 0, s[46:47]
	global_load_dword v139, v[16:17], off nt
	v_lshl_add_u64 v[16:17], v[16:17], 0, s[46:47]
	global_load_dword v140, v[16:17], off nt
	v_lshl_add_u64 v[16:17], v[16:17], 0, s[46:47]
	global_load_dword v141, v[16:17], off nt
	v_lshl_add_u64 v[16:17], v[16:17], 0, s[46:47]
	global_load_dword v142, v[16:17], off nt
	v_lshl_add_u64 v[16:17], v[16:17], 0, s[46:47]
	global_load_dword v143, v[16:17], off nt
	v_lshl_add_u64 v[16:17], v[16:17], 0, s[46:47]
	global_load_dword v144, v[16:17], off nt
	v_lshl_add_u64 v[16:17], v[16:17], 0, s[46:47]
	global_load_dword v146, v[16:17], off nt
	v_lshl_add_u64 v[16:17], v[16:17], 0, s[46:47]
	global_load_dword v147, v[16:17], off nt
	v_lshl_add_u64 v[16:17], v[16:17], 0, s[46:47]
	global_load_dword v148, v[16:17], off nt
	v_lshl_add_u64 v[16:17], v[16:17], 0, s[46:47]
	global_load_dword v149, v[16:17], off nt
	v_lshl_add_u64 v[16:17], v[16:17], 0, s[46:47]
	global_load_dword v151, v[16:17], off nt
	v_lshl_add_u64 v[16:17], v[16:17], 0, s[46:47]
	global_load_dword v152, v[16:17], off nt
	v_lshl_add_u64 v[16:17], v[16:17], 0, s[46:47]
	global_load_dword v153, v[16:17], off nt
	v_lshl_add_u64 v[16:17], v[16:17], 0, s[46:47]
	global_load_dword v154, v[16:17], off nt
	v_lshl_add_u64 v[16:17], v[16:17], 0, s[46:47]
	global_load_dword v155, v[16:17], off nt
	v_lshl_add_u64 v[16:17], v[16:17], 0, s[46:47]
	global_load_dword v157, v[16:17], off nt
	v_lshl_add_u64 v[16:17], v[16:17], 0, s[46:47]
	global_load_dword v158, v[16:17], off nt
	v_lshl_add_u64 v[16:17], v[16:17], 0, s[46:47]
	ds_write2st64_b32 v28, v91, v90 offset0:2 offset1:3
	ds_write2st64_b32 v28, v89, v88 offset0:4 offset1:5
	ds_write2st64_b32 v28, v86, v85 offset0:6 offset1:7
	ds_write2st64_b32 v21, v83, v84 offset0:8 offset1:9
	ds_write2st64_b32 v21, v79, v80 offset0:10 offset1:11
	ds_write2st64_b32 v21, v75, v76 offset0:12 offset1:13
	ds_write2st64_b32 v21, v71, v72 offset0:14 offset1:15
	ds_write2st64_b32 v22, v65, v66 offset0:16 offset1:17
	ds_write2st64_b32 v22, v61, v62 offset0:18 offset1:19
	ds_write2st64_b32 v22, v57, v58 offset0:20 offset1:21
	ds_write2st64_b32 v22, v53, v54 offset0:22 offset1:23
	ds_write2st64_b32 v23, v45, v46 offset0:24 offset1:25
	ds_write2st64_b32 v23, v35, v36 offset0:26 offset1:27
	ds_write2st64_b32 v23, v33, v34 offset0:28 offset1:29
	ds_write2st64_b32 v23, v31, v32 offset0:30 offset1:31
	ds_write2st64_b32 v24, v29, v30 offset0:32 offset1:33
	ds_write2st64_b32 v24, v81, v82 offset0:34 offset1:35
	ds_write2st64_b32 v24, v77, v78 offset0:36 offset1:37
	ds_write2st64_b32 v24, v73, v74 offset0:38 offset1:39
	ds_write2st64_b32 v25, v69, v70 offset0:40 offset1:41
	ds_write2st64_b32 v25, v67, v68 offset0:42 offset1:43
	ds_write2st64_b32 v25, v63, v64 offset0:44 offset1:45
	ds_write2st64_b32 v25, v59, v60 offset0:46 offset1:47
	ds_write2st64_b32 v26, v55, v56 offset0:48 offset1:49
	ds_write2st64_b32 v26, v51, v52 offset0:50 offset1:51
	global_load_dword v159, v[16:17], off nt
	ds_write2st64_b32 v26, v38, v39 offset0:52 offset1:53
	ds_write2st64_b32 v26, v40, v42 offset0:54 offset1:55
	ds_write2st64_b32 v27, v37, v41 offset0:56 offset1:57
	ds_write2st64_b32 v27, v43, v44 offset0:58 offset1:59
	ds_write2st64_b32 v27, v47, v48 offset0:60 offset1:61
	ds_write2st64_b32 v27, v49, v50 offset0:62 offset1:63
	s_waitcnt lgkmcnt(0)
	ds_read2_b32 v[16:17], v1 offset1:32
	v_mov_b32_e32 v30, 0
	ds_read2_b32 v[32:33], v1 offset0:128 offset1:160
	v_mov_b32_e32 v31, 0
	v_add_u32_e32 v145, 0x400, v1
	s_waitcnt lgkmcnt(1)
	v_mul_f32_e32 v4, 0x42800000, v16
	v_mul_f32_e32 v15, 0x42800000, v17
	ds_read2_b32 v[16:17], v1 offset0:64 offset1:96
	v_cvt_pk_fp8_f32 v30, v4, v15
	ds_read2_b32 v[34:35], v145 offset0:128 offset1:160
	v_add_u32_e32 v150, 0x400, v9
	ds_read2_b32 v[38:39], v150 offset0:128 offset1:160
	s_waitcnt lgkmcnt(2)
	v_mul_f32_e32 v4, 0x42800000, v16
	v_mul_f32_e32 v15, 0x42800000, v17
	ds_read2_b32 v[16:17], v1 offset0:192 offset1:224
	v_cvt_pk_fp8_f32 v30, v4, v15 op_sel:[0,0,1]
	v_mul_f32_e32 v4, 0x42800000, v32
	v_mul_f32_e32 v15, 0x42800000, v33
	v_cvt_pk_fp8_f32 v31, v4, v15
	s_waitcnt lgkmcnt(0)
	v_mul_f32_e32 v4, 0x42800000, v16
	v_mul_f32_e32 v15, 0x42800000, v17
	ds_read2_b32 v[16:17], v145 offset0:64 offset1:96
	ds_read2_b32 v[32:33], v145 offset1:32
	v_cvt_pk_fp8_f32 v31, v4, v15 op_sel:[0,0,1]
	v_lshl_add_u64 v[10:11], v[10:11], 0, v[6:7]
	v_add_u32_e32 v156, 0x400, v18
	s_waitcnt lgkmcnt(1)
	v_mul_f32_e32 v29, 0x42800000, v16
	v_mul_f32_e32 v36, 0x42800000, v17
	ds_read2_b32 v[16:17], v145 offset0:192 offset1:224
	s_waitcnt lgkmcnt(1)
	v_mul_f32_e32 v4, 0x42800000, v32
	v_mul_f32_e32 v15, 0x42800000, v33
	v_mov_b32_e32 v32, 0
	v_cvt_pk_fp8_f32 v32, v4, v15
	v_mul_f32_e32 v4, 0x42800000, v34
	v_mul_f32_e32 v15, 0x42800000, v35
	v_mov_b32_e32 v33, 0
	ds_read2_b32 v[34:35], v9 offset1:32
	v_cvt_pk_fp8_f32 v33, v4, v15
	s_waitcnt lgkmcnt(1)
	v_mul_f32_e32 v4, 0x42800000, v16
	v_mul_f32_e32 v15, 0x42800000, v17
	ds_read2_b32 v[16:17], v9 offset0:64 offset1:96
	v_cvt_pk_fp8_f32 v32, v29, v36 op_sel:[0,0,1]
	ds_read2_b32 v[36:37], v9 offset0:128 offset1:160
	v_cvt_pk_fp8_f32 v33, v4, v15 op_sel:[0,0,1]
	s_waitcnt lgkmcnt(2)
	v_mul_f32_e32 v4, 0x42800000, v34
	v_mul_f32_e32 v15, 0x42800000, v35
	v_mov_b32_e32 v34, 0
	v_cvt_pk_fp8_f32 v34, v4, v15
	s_waitcnt lgkmcnt(1)
	v_mul_f32_e32 v4, 0x42800000, v16
	v_mul_f32_e32 v15, 0x42800000, v17
	ds_read2_b32 v[16:17], v9 offset0:192 offset1:224
	s_waitcnt lgkmcnt(1)
	v_mul_f32_e32 v29, 0x42800000, v36
	v_mul_f32_e32 v36, 0x42800000, v37
	v_mov_b32_e32 v35, 0
	v_cvt_pk_fp8_f32 v35, v29, v36
	ds_read2_b32 v[36:37], v150 offset1:32
	v_cvt_pk_fp8_f32 v34, v4, v15 op_sel:[0,0,1]
	s_waitcnt lgkmcnt(1)
	v_mul_f32_e32 v4, 0x42800000, v16
	v_mul_f32_e32 v15, 0x42800000, v17
	ds_read2_b32 v[16:17], v150 offset0:64 offset1:96
	v_cvt_pk_fp8_f32 v35, v4, v15 op_sel:[0,0,1]
	s_waitcnt lgkmcnt(1)
	v_mul_f32_e32 v4, 0x42800000, v36
	v_mul_f32_e32 v15, 0x42800000, v37
	v_mov_b32_e32 v36, 0
	v_cvt_pk_fp8_f32 v36, v4, v15
	s_waitcnt lgkmcnt(0)
	v_mul_f32_e32 v4, 0x42800000, v16
	v_mul_f32_e32 v15, 0x42800000, v17
	ds_read2_b32 v[16:17], v150 offset0:192 offset1:224
	v_cvt_pk_fp8_f32 v36, v4, v15 op_sel:[0,0,1]
	v_mul_f32_e32 v4, 0x42800000, v38
	v_mul_f32_e32 v15, 0x42800000, v39
	v_mov_b32_e32 v37, 0
	v_cvt_pk_fp8_f32 v37, v4, v15
	s_waitcnt lgkmcnt(0)
; __device__ __forceinline__ MoeItem moe_item(const float* wg, const float* wu, const float* wd, const float* win, const float* wout, const float* wpn, const float* wpd, unsigned char* ws, int r, int lane) {
;     ...
;     const int mat = r / MOE_IE, q = r % MOE_IE, e = mat / 3, which = mat % 3, kb = q / 64, nb = q % 64, n0 = nb * 32;
;     const float* src = (which == 0 ? wg : (which == 1 ? wu : wd)) + (size_t)e * DM * DFF + (size_t)(kb * 128 + (lane >> 5)) * DFF + n0 + (lane & 31);
;     unsigned char* dst;
;     if (which < 2) dst = ws + WS_WGUT + ((size_t)(e * 16 + (n0 >> 7)) * 256 + which * 128 + (n0 & 127)) * DM;
;     else dst = ws + WS_WDT + ((size_t)e * DM + n0) * DFF;
;     MoeItem it; it.stride = DFF; it.dpitch = DM; it.src = src; it.dst = dst + kb * 128 + (size_t)(lane >> 3) * DM + 16 * (lane & 7); return it;
	v_mul_f32_e32 v4, 0x42800000, v16
	v_mul_f32_e32 v15, 0x42800000, v17
	ds_read2_b32 v[16:17], v18 offset1:32
	v_cvt_pk_fp8_f32 v37, v4, v15 op_sel:[0,0,1]
	global_store_dwordx4 v[10:11], v[30:33], off nt
	ds_read2_b32 v[32:33], v18 offset0:64 offset1:96
	s_lshl_b64 s[38:39], s[38:39], 3
	s_waitcnt lgkmcnt(1)
	v_mul_f32_e32 v4, 0x42800000, v16
	v_mul_f32_e32 v15, 0x42800000, v17
	ds_read2_b32 v[16:17], v18 offset0:128 offset1:160
	v_mov_b32_e32 v30, 0
	v_cvt_pk_fp8_f32 v30, v4, v15
	s_waitcnt lgkmcnt(1)
	v_mul_f32_e32 v4, 0x42800000, v32
	v_mov_b32_e32 v31, 0
	s_waitcnt lgkmcnt(0)
	v_mul_f32_e32 v29, 0x42800000, v16
	v_mul_f32_e32 v32, 0x42800000, v17
	ds_read2_b32 v[16:17], v18 offset0:192 offset1:224
	v_mul_f32_e32 v15, 0x42800000, v33
	v_cvt_pk_fp8_f32 v31, v29, v32
	ds_read2_b32 v[32:33], v156 offset1:32
	v_cvt_pk_fp8_f32 v30, v4, v15 op_sel:[0,0,1]
	s_waitcnt lgkmcnt(1)
	v_mul_f32_e32 v4, 0x42800000, v16
	v_mul_f32_e32 v15, 0x42800000, v17
	ds_read2_b32 v[16:17], v156 offset0:64 offset1:96
	v_lshl_add_u64 v[10:11], v[10:11], 0, s[38:39]
	global_store_dwordx4 v[10:11], v[34:37], off nt
	ds_read2_b32 v[34:35], v156 offset0:128 offset1:160
	v_cvt_pk_fp8_f32 v31, v4, v15 op_sel:[0,0,1]
	s_waitcnt lgkmcnt(2)
	v_mul_f32_e32 v4, 0x42800000, v32
	v_mul_f32_e32 v15, 0x42800000, v33
	v_mov_b32_e32 v32, 0
	v_cvt_pk_fp8_f32 v32, v4, v15
	s_waitcnt lgkmcnt(1)
	v_mul_f32_e32 v4, 0x42800000, v16
	v_mul_f32_e32 v15, 0x42800000, v17
	ds_read2_b32 v[16:17], v156 offset0:192 offset1:224
	s_waitcnt lgkmcnt(1)
	v_mul_f32_e32 v29, 0x42800000, v34
	v_mul_f32_e32 v34, 0x42800000, v35
	v_mov_b32_e32 v33, 0
	v_cvt_pk_fp8_f32 v33, v29, v34
	ds_read2_b32 v[34:35], v19 offset1:32
	v_cvt_pk_fp8_f32 v32, v4, v15 op_sel:[0,0,1]
	s_waitcnt lgkmcnt(1)
	v_mul_f32_e32 v4, 0x42800000, v16
	v_mul_f32_e32 v15, 0x42800000, v17
	ds_read2_b32 v[16:17], v19 offset0:64 offset1:96
	ds_read2_b32 v[36:37], v19 offset0:128 offset1:160
	v_cvt_pk_fp8_f32 v33, v4, v15 op_sel:[0,0,1]
	s_waitcnt lgkmcnt(2)
	v_mul_f32_e32 v4, 0x42800000, v34
	v_mul_f32_e32 v15, 0x42800000, v35
	v_mov_b32_e32 v34, 0
	v_cvt_pk_fp8_f32 v34, v4, v15
	s_waitcnt lgkmcnt(1)
	v_mul_f32_e32 v4, 0x42800000, v16
	v_mul_f32_e32 v15, 0x42800000, v17
	ds_read2_b32 v[16:17], v19 offset0:192 offset1:224
	s_waitcnt lgkmcnt(1)
	v_mul_f32_e32 v29, 0x42800000, v36
	v_mul_f32_e32 v36, 0x42800000, v37
	v_mov_b32_e32 v35, 0
	v_add_u32_e32 v160, 0x400, v19
	v_cvt_pk_fp8_f32 v35, v29, v36
	ds_read2_b32 v[36:37], v160 offset1:32
	v_cvt_pk_fp8_f32 v34, v4, v15 op_sel:[0,0,1]
	s_waitcnt lgkmcnt(1)
	v_mul_f32_e32 v4, 0x42800000, v16
	v_mul_f32_e32 v15, 0x42800000, v17
	ds_read2_b32 v[16:17], v160 offset0:64 offset1:96
	ds_read2_b32 v[38:39], v160 offset0:128 offset1:160
	v_cvt_pk_fp8_f32 v35, v4, v15 op_sel:[0,0,1]
	s_waitcnt lgkmcnt(2)
	v_mul_f32_e32 v4, 0x42800000, v36
	v_mul_f32_e32 v15, 0x42800000, v37
	v_mov_b32_e32 v36, 0
	v_cvt_pk_fp8_f32 v36, v4, v15
	s_waitcnt lgkmcnt(1)
	v_mul_f32_e32 v4, 0x42800000, v16
	v_mul_f32_e32 v15, 0x42800000, v17
	ds_read2_b32 v[16:17], v160 offset0:192 offset1:224
	s_waitcnt lgkmcnt(1)
	v_mul_f32_e32 v29, 0x42800000, v38
	v_mul_f32_e32 v38, 0x42800000, v39
	v_mov_b32_e32 v37, 0
	v_cvt_pk_fp8_f32 v37, v29, v38
	v_cvt_pk_fp8_f32 v36, v4, v15 op_sel:[0,0,1]
	s_waitcnt lgkmcnt(0)
	v_mul_f32_e32 v4, 0x42800000, v16
	v_mul_f32_e32 v15, 0x42800000, v17
	v_cvt_pk_fp8_f32 v37, v4, v15 op_sel:[0,0,1]
	v_lshl_add_u64 v[10:11], v[10:11], 0, s[38:39]
	global_store_dwordx4 v[10:11], v[30:33], off nt
	v_lshl_add_u64 v[10:11], v[10:11], 0, s[38:39]
	global_store_dwordx4 v[10:11], v[34:37], off nt
	s_waitcnt lgkmcnt(0)
	s_add_i32 s3, s89, s3
	s_min_i32 s43, s3, s7
	s_cmp_lt_i32 s43, 0x19000
	s_mov_b64 s[38:39], -1
	s_cbranch_scc0 .LBB0_126
	s_cmp_lt_i32 s43, 0x18c00
	s_cbranch_scc0 .LBB0_123
	s_cmp_lt_i32 s43, 0x18000
	s_cbranch_scc0 .LBB0_113
	s_ashr_i32 s4, s43, 31
	s_lshr_b32 s4, s4, 22
	s_add_i32 s4, s43, s4
	s_ashr_i32 s39, s4, 10
	s_and_b32 s4, s4, 0xfc00
	s_sub_i32 s46, s43, s4
	s_mul_hi_i32 s4, s43, 0x2aaaaaab
	s_lshr_b32 s38, s4, 31
	s_ashr_i32 s4, s4, 9
	s_add_i32 s38, s4, s38
	s_mul_hi_i32 s4, s39, 0x55555556
	s_lshr_b32 s45, s4, 31
	s_add_i32 s4, s4, s45
	s_mul_i32 s4, s4, 3
	s_sub_i32 s4, s39, s4
	s_sext_i32_i16 s39, s46
	s_bfe_u32 s39, s39, 0x60019
	s_add_i32 s45, s46, s39
	s_and_b32 s39, s45, 0xffc0
	s_sub_i32 s39, s46, s39
	s_sext_i32_i16 s84, s39
	s_lshl_b32 s46, s84, 5
	s_ashr_i32 s39, s38, 31
	s_ashr_i32 s47, s46, 31
	s_cmp_gt_i32 s4, 1
	s_mov_b64 s[70:71], -1
	s_cbranch_scc0 .LBB0_110
	s_lshl_b64 s[68:69], s[38:39], 22
	s_lshl_b64 s[70:71], s[46:47], 11
	s_add_u32 s68, s73, s68
	s_addc_u32 s69, s74, s69
	s_add_u32 s68, s68, s70
	s_addc_u32 s69, s69, s71
	s_mov_b64 s[70:71], 0
